# scan loader: write-through (sc0 sc1) on the bf16 weight-tile stores
# baseline (speedup 1.0000x reference)
; #define LAS __attribute__((address_space(3)))
; __device__ __forceinline__ unsigned cvt_pk_bf16(float lo, float hi) { unsigned r; asm volatile("v_cvt_pk_bf16_f32 %0, %1, %2" : "=v"(r) : "v"(lo), "v"(hi)); return r; }
; __device__ __forceinline__ void p4_scan(const Args& a, const Frame& F) {
;     ...
;                 for (int i = 0; i < 8; ++i) { const int p = ht + 256 * i, row = p >> 4, c16 = p & 15; const int tok = base + (dir ? 127 - row : row);
;                     pq[i] = *(const u32x4*)(QKC + (size_t)tok * 1024 + h * 128 + c16 * 8); pk[i] = *(const u32x4*)(QKC + (size_t)tok * 1024 + 512 + h * 128 + c16 * 8); }
; #pragma unroll
;                 for (int i = 0; i < 2; ++i) { const int p = ht + 256 * i, row = p >> 2, cc = p & 3; const int tok = base + (dir ? 127 - row : row);
;                     pv[i] = *(const u32x4*)(PV + (size_t)tok * 512 + h * 128 + vs * 32 + cc * 8); pga[i] = GS[(size_t)hd * TA + tok]; }
; #pragma unroll
;                 for (int i = 0; i < 2; ++i) { const int idx = ht + 256 * i; if (idx < 384) { const int row = idx & 127, arr = idx >> 7; const int tok = base + (dir ? 127 - row : row); pgl[i] = GS[(size_t)(arr * 8 + hd) * TA + tok]; } }
;                 pbt = CH[(hd * 528 + (base >> 7)) * 2]; ppx = CH[(hd * 528 + (base >> 7)) * 2 + 1];
;             };
;             auto commitK = [&](int kbuf) {
; #pragma unroll
;                 for (int i = 0; i < 8; ++i) { const int p = ht + 256 * i, row = p >> 4, c16 = p & 15; *(LAS u32x4*)(L + kbuf + row * SP + c16 * 16) = pk[i]; } };
;     ...
;             auto conv_store = [&]() {
;                 const bool hi = lane >= 32;
;                 u32x4 o[4];
; #pragma unroll
;                 for (int i = 0; i < 16; ++i) { const float snd = hi ? cv[i] : cv[16 + i]; const float rcv = __shfl_xor(snd, 32);
;                     const unsigned pkd = pg8::cvt_pk_bf16(hi ? rcv : cv[i], hi ? cv[16 + i] : rcv);
;                     if ((i & 3) == 0) o[i >> 2].x = pkd; else if ((i & 3) == 1) o[i >> 2].y = pkd; else if ((i & 3) == 2) o[i >> 2].z = pkd; else o[i >> 2].w = pkd; }
;                 u32x4* dst = (u32x4*)(cD + (size_t)crow * 1024 + ck0 + (hi ? 32 : 0));
; #pragma unroll
;                 for (int j2 = 0; j2 < 4; ++j2) dst[j2] = o[j2];
;             };
.LBB0_496:
	s_or_b64 exec, exec, s[54:55]
	s_ashr_i32 s54, s56, 7
	s_add_i32 s54, s54, s76
	s_lshl_b32 s54, s54, 1
	s_ashr_i32 s55, s54, 31
	s_lshl_b64 s[54:55], s[54:55], 2
	s_add_u32 s54, s60, s54
	s_addc_u32 s55, s61, s55
	global_load_dwordx2 v[94:95], v145, s[54:55]
	s_bitcmp0_b32 s44, 0
	s_cselect_b64 s[54:55], -1, 0
	s_and_b64 s[56:57], s[54:55], exec
	s_cselect_b32 s56, 0x11000, s91
	s_add_i32 s56, s56, 0
	v_add3_u32 v144, s56, v109, v117
	ds_write_b128 v144, v[220:223]
	v_add3_u32 v48, s56, v110, v117
	ds_write_b128 v48, v[224:227]
	v_add3_u32 v48, s56, v111, v117
	ds_write_b128 v48, v[228:231]
	v_add3_u32 v48, s56, v112, v117
	ds_write_b128 v48, v[232:235]
	v_add3_u32 v48, s56, v113, v117
	ds_write_b128 v48, v[236:239]
	v_add3_u32 v48, s56, v114, v117
	ds_write_b128 v48, v[240:243]
	v_add3_u32 v48, s56, v115, v117
	ds_write_b128 v48, v[244:247]
	v_add3_u32 v48, s56, v116, v117
	ds_write_b128 v48, v[248:251]
	s_add_i32 s98, s35, 1
	s_min_i32 s98, s98, 0x41
	s_sub_i32 s99, 0x41, s98
	s_add_i32 s98, s98, -2
	s_and_b64 s[100:101], s[4:5], exec
	s_cselect_b32 s98, s98, s99
	s_lshl_b32 s98, s98, 7
	s_add_i32 s98, s98, s33
	v_add_u32_e32 v214, s98, v96
	v_ashrrev_i32_e32 v215, 31, v214
	v_lshlrev_b64 v[214:215], 11, v[214:215]
	v_lshl_add_u64 v[214:215], v[92:93], 0, v[214:215]
	global_load_dwordx4 v[220:223], v[214:215], off offset:1024
	v_add_u32_e32 v214, s98, v97
	v_ashrrev_i32_e32 v215, 31, v214
	v_lshlrev_b64 v[214:215], 11, v[214:215]
	v_lshl_add_u64 v[214:215], v[92:93], 0, v[214:215]
	global_load_dwordx4 v[224:227], v[214:215], off offset:1024
	v_add_u32_e32 v214, s98, v98
	v_ashrrev_i32_e32 v215, 31, v214
	v_lshlrev_b64 v[214:215], 11, v[214:215]
	v_lshl_add_u64 v[214:215], v[92:93], 0, v[214:215]
	global_load_dwordx4 v[228:231], v[214:215], off offset:1024
	v_add_u32_e32 v214, s98, v99
	v_ashrrev_i32_e32 v215, 31, v214
	v_lshlrev_b64 v[214:215], 11, v[214:215]
	v_lshl_add_u64 v[214:215], v[92:93], 0, v[214:215]
	global_load_dwordx4 v[232:235], v[214:215], off offset:1024
	v_add_u32_e32 v214, s98, v100
	v_ashrrev_i32_e32 v215, 31, v214
	v_lshlrev_b64 v[214:215], 11, v[214:215]
	v_lshl_add_u64 v[214:215], v[92:93], 0, v[214:215]
	global_load_dwordx4 v[236:239], v[214:215], off offset:1024
	v_add_u32_e32 v214, s98, v101
	v_ashrrev_i32_e32 v215, 31, v214
	v_lshlrev_b64 v[214:215], 11, v[214:215]
	v_lshl_add_u64 v[214:215], v[92:93], 0, v[214:215]
	global_load_dwordx4 v[240:243], v[214:215], off offset:1024
	v_add_u32_e32 v214, s98, v102
	v_ashrrev_i32_e32 v215, 31, v214
	v_lshlrev_b64 v[214:215], 11, v[214:215]
	v_lshl_add_u64 v[214:215], v[92:93], 0, v[214:215]
	global_load_dwordx4 v[244:247], v[214:215], off offset:1024
	v_add_u32_e32 v214, s98, v103
	v_ashrrev_i32_e32 v215, 31, v214
	v_lshlrev_b64 v[214:215], 11, v[214:215]
	v_lshl_add_u64 v[214:215], v[92:93], 0, v[214:215]
	global_load_dwordx4 v[248:251], v[214:215], off offset:1024
	s_waitcnt vmcnt(21)
	s_cmp_gt_u32 s44, 47
	s_cbranch_scc1 .LBB0_498
	v_cvt_pk_bf16_f32 v48, v174, v178
	v_cvt_pk_bf16_f32 v49, v182, v138
	v_cvt_pk_bf16_f32 v50, v148, v198
	v_cvt_pk_bf16_f32 v51, v202, v210
	v_cvt_pk_bf16_f32 v52, v175, v179
	v_cvt_pk_bf16_f32 v53, v183, v139
	v_cvt_pk_bf16_f32 v54, v149, v199
	v_cvt_pk_bf16_f32 v55, v203, v211
	v_cvt_pk_bf16_f32 v56, v176, v180
	v_cvt_pk_bf16_f32 v57, v184, v140
	v_cvt_pk_bf16_f32 v58, v150, v200
	v_cvt_pk_bf16_f32 v59, v204, v212
	v_cvt_pk_bf16_f32 v60, v177, v181
	v_cvt_pk_bf16_f32 v61, v185, v141
	v_cvt_pk_bf16_f32 v62, v151, v201
	v_cvt_pk_bf16_f32 v63, v205, v213
	v_add_u32_e32 v80, v80, v206
	v_ashrrev_i32_e32 v81, 31, v80
	v_lshlrev_b64 v[64:65], 11, v[80:81]
	v_lshl_add_u64 v[64:65], s[52:53], 0, v[64:65]
	v_add_u32_e32 v82, v82, v207
	v_mov_b32_e32 v83, v145
	v_lshl_add_u64 v[64:65], v[82:83], 1, v[64:65]
	s_mov_b64 s[100:101], 0x1000
	global_store_dwordx4 v[64:65], v[48:51], off sc0 sc1
	global_store_dwordx4 v[64:65], v[52:55], off offset:2048 sc0 sc1
	s_nop 1
	v_lshl_add_u64 v[64:65], s[100:101], 0, v[64:65]
	global_store_dwordx4 v[64:65], v[56:59], off sc0 sc1
	global_store_dwordx4 v[64:65], v[60:63], off offset:2048 sc0 sc1
